# barrier acquire: L1-only invalidate (buffer_inv sc0) after the poll; the 32 per-XCD L2 invalidates serialized at ~54ns each and local VRAM is MTYPE RW (kept coherent in L2 by probes). Plus leader->TOP
# speedup vs baseline: 1.0240x; 1.0236x over previous
; __device__ __forceinline__ unsigned xb_ld(unsigned* p)              { return __hip_atomic_load(p, __ATOMIC_RELAXED, __HIP_MEMORY_SCOPE_AGENT); }
; __device__ __forceinline__ unsigned xb_add(unsigned* p, unsigned v) { return __hip_atomic_fetch_add(p, v, __ATOMIC_RELAXED, __HIP_MEMORY_SCOPE_AGENT); }
; #define XB_SPIN(cond, bar) do { unsigned _sp = 0; while (cond) { __builtin_amdgcn_s_sleep(1); \
;     if ((++_sp & 255u) == 0u) { if (xb_ld(&(bar)[XB_TMO])) break; if (_sp > XB_SPIN_CAP) { atomicAdd(&(bar)[XB_TMO], 1u); break; } } } } while (0)
; __device__ __forceinline__ void xcd_barrier(const XcdBarrier& b, int wid0) {
;     ...
;             else XB_SPIN(xb_ld(&bar[XB_TOPGEN]) == tg, bar);
;             (void)xb_add(&bar[XB_XGEN(b.x)], 1u);
;             __builtin_amdgcn_fence(__ATOMIC_ACQUIRE, "agent");
;             asm volatile("s_waitcnt vmcnt(0)" ::: "memory");
;         } else {
;             XB_SPIN(xb_ld(&bar[XB_XGEN(b.x)]) == gen, bar);
;             __builtin_amdgcn_fence(__ATOMIC_ACQUIRE, "agent");
;             asm volatile("s_waitcnt vmcnt(0)" ::: "memory");
;         }
.Lxb0_done:
	buffer_inv sc0
	s_waitcnt vmcnt(0)

; __device__ __forceinline__ unsigned xb_ld(unsigned* p)              { return __hip_atomic_load(p, __ATOMIC_RELAXED, __HIP_MEMORY_SCOPE_AGENT); }
; __device__ __forceinline__ unsigned xb_add(unsigned* p, unsigned v) { return __hip_atomic_fetch_add(p, v, __ATOMIC_RELAXED, __HIP_MEMORY_SCOPE_AGENT); }
; #define XB_SPIN(cond, bar) do { unsigned _sp = 0; while (cond) { __builtin_amdgcn_s_sleep(1); \
;     if ((++_sp & 255u) == 0u) { if (xb_ld(&(bar)[XB_TMO])) break; if (_sp > XB_SPIN_CAP) { atomicAdd(&(bar)[XB_TMO], 1u); break; } } } } while (0)
; __device__ __forceinline__ void xcd_barrier(const XcdBarrier& b, int wid0) {
;     ...
;             else XB_SPIN(xb_ld(&bar[XB_TOPGEN]) == tg, bar);
;             (void)xb_add(&bar[XB_XGEN(b.x)], 1u);
;             __builtin_amdgcn_fence(__ATOMIC_ACQUIRE, "agent");
;             asm volatile("s_waitcnt vmcnt(0)" ::: "memory");
;         } else {
;             XB_SPIN(xb_ld(&bar[XB_XGEN(b.x)]) == gen, bar);
;             __builtin_amdgcn_fence(__ATOMIC_ACQUIRE, "agent");
;             asm volatile("s_waitcnt vmcnt(0)" ::: "memory");
;         }
.Lxb3_done:
	buffer_inv sc0
	s_waitcnt vmcnt(0)
	s_branch .LBB0_805
